# v14: v13 + unary kernel prologue de-serialisation (all kernargs at once, pm-row loads in parallel with tile-info load)
# baseline (speedup 1.0000x reference)
.LBB7_4:
	s_andn2_b64 vcc, exec, s[6:7]
	s_cbranch_vccnz .LBB7_11
	s_cmpk_gt_i32 s4, 0x1fe
	s_cbranch_scc1 .LBB7_11
	s_load_dwordx2 s[2:3], s[0:1], 0x18
	s_load_dwordx2 s[18:19], s[0:1], 0x10
	s_load_dwordx4 s[20:23], s[0:1], 0x0
	s_load_dwordx2 s[12:13], s[0:1], 0x20
	s_load_dwordx2 s[24:25], s[0:1], 0x30
	s_ashr_i32 s5, s4, 31
	s_lshl_b64 s[6:7], s[4:5], 2
	s_lshl_b32 s16, s4, 6
	s_ashr_i32 s17, s16, 31
	s_lshl_b64 s[16:17], s[16:17], 2
	v_lshrrev_b32_e32 v1, 4, v0
	v_lshlrev_b32_e32 v3, 2, v1
	s_waitcnt lgkmcnt(0)
	s_add_u32 s26, s2, s6
	s_addc_u32 s27, s3, s7
	s_load_dword s11, s[26:27], 0x0
	s_add_u32 s2, s18, s16
	s_addc_u32 s3, s19, s17
	global_load_dword v2, v3, s[2:3]
	global_load_dword v4, v3, s[2:3] offset:128
	s_waitcnt lgkmcnt(0)
	s_cmp_lt_i32 s11, 0
	s_cbranch_scc1 .LBB7_11
	s_mov_b64 s[4:5], s[20:21]
	s_mov_b64 s[6:7], s[22:23]
	s_mov_b64 s[8:9], s[24:25]
	v_and_b32_e32 v96, 15, v0
	v_mov_b32_e32 v25, 0
	v_lshlrev_b32_e32 v24, 4, v96
	s_and_b32 s1, s11, 0xff
	v_lshl_add_u64 v[6:7], s[4:5], 0, v[24:25]
	s_lshr_b32 s4, s11, 8
	s_lshl_b32 s0, s1, 21
	s_waitcnt lgkmcnt(0)
	s_add_u32 s12, s12, s0
	s_addc_u32 s13, s13, 0
	s_lshl_b32 s0, s10, 7
	v_or_b32_e32 v8, s0, v1
	v_ashrrev_i32_e32 v9, 31, v8
	v_lshlrev_b64 v[8:9], 11, v[8:9]
	v_lshl_add_u64 v[8:9], s[12:13], 0, v[8:9]
	s_mov_b32 s14, 0x10000
	v_lshl_add_u64 v[8:9], v[8:9], 0, v[24:25]
	v_add_co_u32_e32 v10, vcc, s14, v8
	s_mov_b32 s15, 0x20000
	s_nop 0
	v_addc_co_u32_e32 v11, vcc, 0, v9, vcc
	v_add_co_u32_e32 v12, vcc, s15, v8
	s_mov_b32 s16, 0x30000
	s_nop 0
	v_addc_co_u32_e32 v13, vcc, 0, v9, vcc
	v_add_co_u32_e32 v14, vcc, s16, v8
	global_load_dwordx4 v[32:35], v[8:9], off
	s_nop 0
	v_addc_co_u32_e32 v15, vcc, 0, v9, vcc
	global_load_dwordx4 v[36:39], v[10:11], off
	global_load_dwordx4 v[40:43], v[12:13], off
	global_load_dwordx4 v[44:47], v[14:15], off
	v_bfe_u32 v30, v0, 6, 2
	v_bfe_u32 v29, v0, 4, 2
	s_movk_i32 s5, 0xf0
	s_lshl_b32 s1, s1, 12
	v_lshlrev_b32_e32 v21, 8, v96
	v_lshlrev_b32_e32 v24, 7, v30
	s_waitcnt vmcnt(5)
	v_ashrrev_i32_e32 v3, 31, v2
	s_waitcnt vmcnt(4)
	v_ashrrev_i32_e32 v5, 31, v4
	v_lshlrev_b64 v[2:3], 11, v[2:3]
	v_lshlrev_b64 v[4:5], 11, v[4:5]
	v_lshl_add_u64 v[16:17], v[6:7], 0, v[2:3]
	v_lshl_add_u64 v[18:19], v[6:7], 0, v[4:5]
	global_load_dwordx4 v[48:51], v[16:17], off
	global_load_dwordx4 v[52:55], v[18:19], off
	global_load_dwordx4 v[56:59], v[16:17], off offset:256
	global_load_dwordx4 v[60:63], v[18:19], off offset:256
	global_load_dwordx4 v[64:67], v[8:9], off offset:256
	global_load_dwordx4 v[68:71], v[10:11], off offset:256
	global_load_dwordx4 v[72:75], v[12:13], off offset:256
	global_load_dwordx4 v[76:79], v[14:15], off offset:256
	v_lshrrev_b32_e32 v2, 8, v0
	v_xor_b32_e32 v0, v1, v0
	v_lshlrev_b32_e32 v3, 8, v1
	v_lshlrev_b32_e32 v0, 4, v0
	v_and_or_b32 v0, v0, s5, v3
	s_add_u32 s5, s8, s1
	s_addc_u32 s10, s9, 0
	s_ashr_i32 s1, s0, 31
	s_lshl_b64 s[8:9], s[0:1], 2
	s_add_u32 s8, s5, s8
	v_lshlrev_b32_e32 v4, 13, v30
	v_bitop3_b32 v1, v1, v96, 3 bitop3:0x6c
	s_addc_u32 s9, s10, s9
	v_lshl_or_b32 v27, v2, 5, v96
	v_add3_u32 v97, 0, v4, v21
	v_lshlrev_b32_e32 v100, 4, v1
	v_add_u32_e32 v20, 0, v0
	v_lshl_add_u64 v[0:1], s[8:9], 0, v[24:25]
	v_lshlrev_b32_e32 v24, 4, v29
	v_lshlrev_b32_e32 v28, 2, v27
	v_add_u32_e32 v31, v97, v100
	v_lshl_add_u64 v[22:23], v[0:1], 0, v[24:25]
	v_lshlrev_b32_e32 v80, 13, v2
	global_load_dword v26, v28, s[2:3] offset:64
	global_load_dwordx4 v[4:7], v[22:23], off
	global_load_dwordx4 v[0:3], v[22:23], off offset:64
	v_bitop3_b32 v23, v29, v96, 4 bitop3:0x36
	v_lshlrev_b32_e32 v101, 4, v23
	v_add3_u32 v22, 0, v80, v21
	v_add_u32_e32 v21, v22, v100
	v_add_u32_e32 v23, v22, v101
	v_bitop3_b32 v24, v29, v96, 8 bitop3:0x36
	v_lshlrev_b32_e32 v102, 4, v24
	v_add_u32_e32 v24, v22, v102
	v_add_u32_e32 v104, 0x8000, v97
	v_add_u32_e32 v116, 0x8000, v20
	s_lshl_b64 s[0:1], s[0:1], 1
	s_add_u32 s0, s6, s0
	s_addc_u32 s1, s7, s1
	v_cmp_gt_u32_e32 vcc, s4, v27
	s_waitcnt vmcnt(14)
	ds_write_b128 v20, v[32:35] offset:32768
	s_waitcnt vmcnt(13)
	ds_write_b128 v20, v[36:39] offset:40960
	s_waitcnt vmcnt(12)
	ds_write_b128 v20, v[40:43] offset:49152
	s_waitcnt vmcnt(11)
	ds_write_b128 v20, v[44:47] offset:57344
	s_waitcnt vmcnt(10)
	ds_write_b128 v20, v[48:51]
	s_waitcnt vmcnt(9)
	ds_write_b128 v20, v[52:55] offset:8192
	s_waitcnt lgkmcnt(0)
	s_barrier
	ds_read_b128 v[34:37], v31 offset:32768
	v_add_u32_e32 v32, v97, v101
	ds_read_b128 v[38:41], v31 offset:36864
	ds_read_b128 v[42:45], v21
	ds_read_b128 v[46:49], v21 offset:4096
	ds_read_b128 v[80:83], v32 offset:32768
	ds_read_b128 v[88:91], v23
	ds_read_b128 v[92:95], v32 offset:36864
	s_waitcnt lgkmcnt(4)
	v_mfma_f32_16x16x32_f16 v[50:53], v[34:37], v[42:45], 0
	v_bitop3_b32 v33, v29, v96, 12 bitop3:0x36
	v_lshlrev_b32_e32 v103, 4, v33
	v_add_u32_e32 v33, v97, v103
	v_mfma_f32_16x16x32_f16 v[42:45], v[38:41], v[42:45], 0
	v_add_u32_e32 v22, v22, v103
	s_waitcnt lgkmcnt(3)
	v_mfma_f32_16x16x32_f16 v[84:87], v[34:37], v[46:49], 0
	v_add_u32_e32 v35, v97, v102
	v_add_u32_e32 v34, v104, v100
	v_mfma_f32_16x16x32_f16 v[36:39], v[38:41], v[46:49], 0
	ds_read_b128 v[46:49], v23 offset:4096
	s_waitcnt lgkmcnt(2)
	v_mfma_f32_16x16x32_f16 v[50:53], v[80:83], v[88:91], v[50:53]
	s_waitcnt lgkmcnt(1)
	v_mfma_f32_16x16x32_f16 v[40:43], v[92:95], v[88:91], v[42:45]
	ds_read_b128 v[88:91], v35 offset:32768
	s_waitcnt lgkmcnt(1)
	v_mfma_f32_16x16x32_f16 v[80:83], v[80:83], v[46:49], v[84:87]
	s_nop 2
	ds_read_b128 v[84:87], v24
	ds_read_b128 v[96:99], v35 offset:36864
	v_mfma_f32_16x16x32_f16 v[36:39], v[92:95], v[46:49], v[36:39]
	ds_read_b128 v[44:47], v24 offset:4096
	s_waitcnt lgkmcnt(2)
	v_mfma_f32_16x16x32_f16 v[48:51], v[88:91], v[84:87], v[50:53]
	s_nop 2
	ds_read_b128 v[52:55], v22
	ds_read_b128 v[92:95], v22 offset:4096
	s_waitcnt vmcnt(8)
	ds_write_b128 v20, v[56:59] offset:16384
	s_waitcnt lgkmcnt(4)
	v_mfma_f32_16x16x32_f16 v[40:43], v[96:99], v[84:87], v[40:43]
	ds_read_b128 v[56:59], v33 offset:32768
	ds_read_b128 v[84:87], v33 offset:36864
	s_waitcnt vmcnt(7)
	ds_write_b128 v20, v[60:63] offset:24576
	s_waitcnt vmcnt(6)
	ds_write_b128 v116, v[64:67] offset:32768
	s_waitcnt vmcnt(5)
	ds_write_b128 v116, v[68:71] offset:40960
	s_waitcnt vmcnt(4)
	ds_write_b128 v116, v[72:75] offset:49152
	s_waitcnt lgkmcnt(9)
	v_mfma_f32_16x16x32_f16 v[60:63], v[88:91], v[44:47], v[80:83]
	s_waitcnt vmcnt(3)
	ds_write_b128 v116, v[76:79] offset:57344
	v_mfma_f32_16x16x32_f16 v[36:39], v[96:99], v[44:47], v[36:39]
	global_load_dwordx4 v[44:47], v[16:17], off offset:512
	global_load_dwordx4 v[64:67], v[18:19], off offset:512
	global_load_dwordx4 v[68:71], v[8:9], off offset:512
	global_load_dwordx4 v[72:75], v[10:11], off offset:512
	global_load_dwordx4 v[76:79], v[12:13], off offset:512
	global_load_dwordx4 v[80:83], v[14:15], off offset:512
	s_waitcnt lgkmcnt(0)
	v_mfma_f32_16x16x32_f16 v[48:51], v[56:59], v[52:55], v[48:51]
	s_barrier
	v_mfma_f32_16x16x32_f16 v[40:43], v[84:87], v[52:55], v[40:43]
	v_mfma_f32_16x16x32_f16 v[52:55], v[56:59], v[92:95], v[60:63]
	ds_read_b128 v[56:59], v34 offset:32768
	s_nop 1
	ds_read_b128 v[60:63], v34 offset:36864
	v_mfma_f32_16x16x32_f16 v[84:87], v[84:87], v[92:95], v[36:39]
	s_nop 2
	ds_read_b128 v[36:39], v21 offset:16384
	ds_read_b128 v[88:91], v21 offset:20480
	s_waitcnt lgkmcnt(1)
	v_mfma_f32_16x16x32_f16 v[48:51], v[56:59], v[36:39], v[48:51]
	v_mfma_f32_16x16x32_f16 v[38:41], v[60:63], v[36:39], v[40:43]
	v_add_u32_e32 v36, v104, v101
	v_add_u32_e32 v37, v104, v102
	s_waitcnt lgkmcnt(0)
	v_mfma_f32_16x16x32_f16 v[52:55], v[56:59], v[88:91], v[52:55]
	ds_read_b128 v[56:59], v36 offset:32768
	ds_read_b128 v[92:95], v36 offset:36864
	v_mfma_f32_16x16x32_f16 v[60:63], v[60:63], v[88:91], v[84:87]
	s_nop 2
	ds_read_b128 v[84:87], v23 offset:16384
	ds_read_b128 v[88:91], v23 offset:20480
	s_waitcnt lgkmcnt(1)
	v_mfma_f32_16x16x32_f16 v[48:51], v[56:59], v[84:87], v[48:51]
	v_mfma_f32_16x16x32_f16 v[38:41], v[92:95], v[84:87], v[38:41]
	s_waitcnt lgkmcnt(0)
	v_mfma_f32_16x16x32_f16 v[52:55], v[56:59], v[88:91], v[52:55]
	ds_read_b128 v[56:59], v37 offset:32768
	ds_read_b128 v[84:87], v37 offset:36864
	v_mfma_f32_16x16x32_f16 v[60:63], v[92:95], v[88:91], v[60:63]
	ds_read_b128 v[88:91], v24 offset:16384
	ds_read_b128 v[92:95], v24 offset:20480
	s_waitcnt lgkmcnt(1)
	v_mfma_f32_16x16x32_f16 v[40:43], v[84:87], v[88:91], v[38:41]
	s_nop 2
	v_add_u32_e32 v38, v104, v103
	v_mfma_f32_16x16x32_f16 v[48:51], v[56:59], v[88:91], v[48:51]
	s_waitcnt lgkmcnt(0)
	v_mfma_f32_16x16x32_f16 v[52:55], v[56:59], v[92:95], v[52:55]
	ds_read_b128 v[56:59], v38 offset:32768
	ds_read_b128 v[88:91], v38 offset:36864
	global_load_dwordx4 v[96:99], v[16:17], off offset:768
	v_mfma_f32_16x16x32_f16 v[60:63], v[84:87], v[92:95], v[60:63]
	ds_read_b128 v[84:87], v22 offset:16384
	ds_read_b128 v[92:95], v22 offset:20480
	global_load_dwordx4 v[100:103], v[18:19], off offset:768
	global_load_dwordx4 v[104:107], v[8:9], off offset:768
	global_load_dwordx4 v[108:111], v[10:11], off offset:768
	global_load_dwordx4 v[112:115], v[12:13], off offset:768
	s_waitcnt lgkmcnt(1)
	v_mfma_f32_16x16x32_f16 v[48:51], v[56:59], v[84:87], v[48:51]
	v_mfma_f32_16x16x32_f16 v[40:43], v[88:91], v[84:87], v[40:43]
	global_load_dwordx4 v[84:87], v[14:15], off offset:768
	s_waitcnt vmcnt(11)
	ds_write_b128 v20, v[44:47]
	s_waitcnt vmcnt(10)
	ds_write_b128 v20, v[64:67] offset:8192
	s_waitcnt vmcnt(9)
	ds_write_b128 v20, v[68:71] offset:32768
	s_waitcnt vmcnt(8)
	ds_write_b128 v20, v[72:75] offset:40960
	s_waitcnt vmcnt(7)
	ds_write_b128 v20, v[76:79] offset:49152
	s_waitcnt vmcnt(6)
	ds_write_b128 v20, v[80:83] offset:57344
	s_waitcnt lgkmcnt(0)
	s_barrier
	ds_read_b128 v[44:47], v31 offset:32768
	v_mfma_f32_16x16x32_f16 v[52:55], v[56:59], v[92:95], v[52:55]
	v_mfma_f32_16x16x32_f16 v[56:59], v[88:91], v[92:95], v[60:63]
	s_nop 2
	ds_read_b128 v[60:63], v31 offset:36864
	ds_read_b128 v[64:67], v21
	ds_read_b128 v[68:71], v21 offset:4096
	s_waitcnt lgkmcnt(1)
	v_mfma_f32_16x16x32_f16 v[48:51], v[44:47], v[64:67], v[48:51]
	v_mfma_f32_16x16x32_f16 v[40:43], v[60:63], v[64:67], v[40:43]
	s_waitcnt lgkmcnt(0)
	v_mfma_f32_16x16x32_f16 v[44:47], v[44:47], v[68:71], v[52:55]
	s_nop 2
	ds_read_b128 v[52:55], v32 offset:32768
	ds_read_b128 v[64:67], v32 offset:36864
	v_mfma_f32_16x16x32_f16 v[56:59], v[60:63], v[68:71], v[56:59]
	ds_read_b128 v[60:63], v23
	ds_read_b128 v[68:71], v23 offset:4096
	s_waitcnt lgkmcnt(1)
	v_mfma_f32_16x16x32_f16 v[48:51], v[52:55], v[60:63], v[48:51]
	v_mfma_f32_16x16x32_f16 v[40:43], v[64:67], v[60:63], v[40:43]
	s_waitcnt lgkmcnt(0)
	v_mfma_f32_16x16x32_f16 v[44:47], v[52:55], v[68:71], v[44:47]
	ds_read_b128 v[52:55], v35 offset:32768
	ds_read_b128 v[60:63], v35 offset:36864
	v_mfma_f32_16x16x32_f16 v[56:59], v[64:67], v[68:71], v[56:59]
	ds_read_b128 v[64:67], v24
	ds_read_b128 v[68:71], v24 offset:4096
	ds_read_b128 v[72:75], v22
	ds_read_b128 v[76:79], v22 offset:4096
	s_waitcnt vmcnt(5)
	ds_write_b128 v20, v[96:99] offset:16384
	s_waitcnt lgkmcnt(4)
	v_mfma_f32_16x16x32_f16 v[48:51], v[52:55], v[64:67], v[48:51]
	v_mfma_f32_16x16x32_f16 v[40:43], v[60:63], v[64:67], v[40:43]
	ds_read_b128 v[64:67], v33 offset:32768
	ds_read_b128 v[80:83], v33 offset:36864
	s_waitcnt vmcnt(4)
	ds_write_b128 v20, v[100:103] offset:24576
	s_waitcnt vmcnt(3)
	ds_write_b128 v116, v[104:107] offset:32768
	s_waitcnt vmcnt(2)
	ds_write_b128 v116, v[108:111] offset:40960
	s_waitcnt vmcnt(1)
	ds_write_b128 v116, v[112:115] offset:49152
	s_waitcnt lgkmcnt(9)
	v_mfma_f32_16x16x32_f16 v[44:47], v[52:55], v[68:71], v[44:47]
	s_waitcnt vmcnt(0)
	ds_write_b128 v116, v[84:87] offset:57344
	v_mfma_f32_16x16x32_f16 v[52:55], v[60:63], v[68:71], v[56:59]
	s_nop 2
	global_load_dwordx4 v[56:59], v[16:17], off offset:1024
	global_load_dwordx4 v[60:63], v[18:19], off offset:1024
	global_load_dwordx4 v[68:71], v[8:9], off offset:1024
	global_load_dwordx4 v[84:87], v[10:11], off offset:1024
	global_load_dwordx4 v[88:91], v[12:13], off offset:1024
	global_load_dwordx4 v[92:95], v[14:15], off offset:1024
	s_waitcnt lgkmcnt(0)
	v_mfma_f32_16x16x32_f16 v[48:51], v[64:67], v[72:75], v[48:51]
	s_barrier
	v_mfma_f32_16x16x32_f16 v[40:43], v[80:83], v[72:75], v[40:43]
	v_mfma_f32_16x16x32_f16 v[44:47], v[64:67], v[76:79], v[44:47]
	ds_read_b128 v[64:67], v34 offset:32768
	ds_read_b128 v[72:75], v34 offset:36864
	v_mfma_f32_16x16x32_f16 v[52:55], v[80:83], v[76:79], v[52:55]
	ds_read_b128 v[76:79], v21 offset:16384
	ds_read_b128 v[80:83], v21 offset:20480
	s_waitcnt lgkmcnt(1)
	v_mfma_f32_16x16x32_f16 v[48:51], v[64:67], v[76:79], v[48:51]
	v_mfma_f32_16x16x32_f16 v[40:43], v[72:75], v[76:79], v[40:43]
	s_waitcnt lgkmcnt(0)
	v_mfma_f32_16x16x32_f16 v[44:47], v[64:67], v[80:83], v[44:47]
	ds_read_b128 v[64:67], v36 offset:32768
	ds_read_b128 v[76:79], v36 offset:36864
	v_mfma_f32_16x16x32_f16 v[52:55], v[72:75], v[80:83], v[52:55]
	ds_read_b128 v[72:75], v23 offset:16384
	ds_read_b128 v[80:83], v23 offset:20480
	s_waitcnt lgkmcnt(1)
	v_mfma_f32_16x16x32_f16 v[48:51], v[64:67], v[72:75], v[48:51]
	v_mfma_f32_16x16x32_f16 v[40:43], v[76:79], v[72:75], v[40:43]
	s_waitcnt lgkmcnt(0)
	v_mfma_f32_16x16x32_f16 v[44:47], v[64:67], v[80:83], v[44:47]
	ds_read_b128 v[64:67], v37 offset:32768
	ds_read_b128 v[72:75], v37 offset:36864
	v_mfma_f32_16x16x32_f16 v[52:55], v[76:79], v[80:83], v[52:55]
	ds_read_b128 v[76:79], v24 offset:16384
	ds_read_b128 v[80:83], v24 offset:20480
	s_waitcnt lgkmcnt(1)
	v_mfma_f32_16x16x32_f16 v[48:51], v[64:67], v[76:79], v[48:51]
	v_mfma_f32_16x16x32_f16 v[40:43], v[72:75], v[76:79], v[40:43]
	s_waitcnt lgkmcnt(0)
	v_mfma_f32_16x16x32_f16 v[44:47], v[64:67], v[80:83], v[44:47]
	ds_read_b128 v[64:67], v38 offset:32768
	ds_read_b128 v[76:79], v22 offset:16384
	ds_read_b128 v[96:99], v38 offset:36864
	global_load_dwordx4 v[100:103], v[10:11], off offset:1280
	v_mfma_f32_16x16x32_f16 v[52:55], v[72:75], v[80:83], v[52:55]
	global_load_dwordx4 v[72:75], v[8:9], off offset:1280
	ds_read_b128 v[80:83], v22 offset:20480
	global_load_dwordx4 v[104:107], v[12:13], off offset:1280
	global_load_dwordx4 v[108:111], v[14:15], off offset:1280
	s_waitcnt lgkmcnt(2)
	v_mfma_f32_16x16x32_f16 v[48:51], v[64:67], v[76:79], v[48:51]
	s_waitcnt lgkmcnt(1)
	v_mfma_f32_16x16x32_f16 v[40:43], v[96:99], v[76:79], v[40:43]
	global_load_dwordx4 v[76:79], v[16:17], off offset:1280
	global_load_dwordx4 v[112:115], v[18:19], off offset:1280
	s_waitcnt vmcnt(11)
	ds_write_b128 v20, v[56:59]
	s_waitcnt vmcnt(10)
	ds_write_b128 v20, v[60:63] offset:8192
	s_waitcnt vmcnt(9)
	ds_write_b128 v20, v[68:71] offset:32768
	s_waitcnt vmcnt(8)
	ds_write_b128 v20, v[84:87] offset:40960
	s_waitcnt vmcnt(7)
	ds_write_b128 v20, v[88:91] offset:49152
	s_waitcnt vmcnt(6)
	ds_write_b128 v20, v[92:95] offset:57344
	s_waitcnt lgkmcnt(0)
	s_barrier
	ds_read_b128 v[56:59], v31 offset:32768
	v_mfma_f32_16x16x32_f16 v[44:47], v[64:67], v[80:83], v[44:47]
	ds_read_b128 v[60:63], v31 offset:36864
	ds_read_b128 v[64:67], v21
	ds_read_b128 v[68:71], v21 offset:4096
	v_mfma_f32_16x16x32_f16 v[52:55], v[96:99], v[80:83], v[52:55]
	s_waitcnt lgkmcnt(1)
	v_mfma_f32_16x16x32_f16 v[48:51], v[56:59], v[64:67], v[48:51]
	v_mfma_f32_16x16x32_f16 v[40:43], v[60:63], v[64:67], v[40:43]
	s_waitcnt lgkmcnt(0)
	v_mfma_f32_16x16x32_f16 v[44:47], v[56:59], v[68:71], v[44:47]
	ds_read_b128 v[56:59], v32 offset:32768
	ds_read_b128 v[64:67], v32 offset:36864
	v_mfma_f32_16x16x32_f16 v[52:55], v[60:63], v[68:71], v[52:55]
	ds_read_b128 v[60:63], v23
	ds_read_b128 v[68:71], v23 offset:4096
	s_waitcnt lgkmcnt(1)
	v_mfma_f32_16x16x32_f16 v[48:51], v[56:59], v[60:63], v[48:51]
	v_mfma_f32_16x16x32_f16 v[40:43], v[64:67], v[60:63], v[40:43]
	s_waitcnt lgkmcnt(0)
	v_mfma_f32_16x16x32_f16 v[44:47], v[56:59], v[68:71], v[44:47]
	ds_read_b128 v[56:59], v35 offset:32768
	ds_read_b128 v[60:63], v35 offset:36864
	v_mfma_f32_16x16x32_f16 v[52:55], v[64:67], v[68:71], v[52:55]
	ds_read_b128 v[64:67], v24
	ds_read_b128 v[68:71], v24 offset:4096
	s_waitcnt vmcnt(4)
	ds_write_b128 v116, v[72:75] offset:32768
	s_waitcnt lgkmcnt(2)
	v_mfma_f32_16x16x32_f16 v[48:51], v[56:59], v[64:67], v[48:51]
	v_mfma_f32_16x16x32_f16 v[40:43], v[60:63], v[64:67], v[40:43]
	ds_read_b128 v[64:67], v33 offset:32768
	s_waitcnt lgkmcnt(2)
	v_mfma_f32_16x16x32_f16 v[44:47], v[56:59], v[68:71], v[44:47]
	ds_read_b128 v[56:59], v22
	ds_read_b128 v[72:75], v33 offset:36864
	ds_write_b128 v116, v[100:103] offset:40960
	s_waitcnt vmcnt(3)
	ds_write_b128 v116, v[104:107] offset:49152
	v_mfma_f32_16x16x32_f16 v[52:55], v[60:63], v[68:71], v[52:55]
	ds_read_b128 v[60:63], v22 offset:4096
	s_waitcnt vmcnt(2)
	ds_write_b128 v116, v[108:111] offset:57344
	s_waitcnt vmcnt(1)
	ds_write_b128 v20, v[76:79] offset:16384
	s_waitcnt vmcnt(0)
	ds_write_b128 v20, v[112:115] offset:24576
	s_waitcnt lgkmcnt(7)
	v_mfma_f32_16x16x32_f16 v[48:51], v[64:67], v[56:59], v[48:51]
	s_waitcnt lgkmcnt(6)
	v_mfma_f32_16x16x32_f16 v[40:43], v[72:75], v[56:59], v[40:43]
	global_load_dwordx4 v[56:59], v[16:17], off offset:1536
	global_load_dwordx4 v[68:71], v[18:19], off offset:1536
	global_load_dwordx4 v[76:79], v[8:9], off offset:1536
	global_load_dwordx4 v[80:83], v[10:11], off offset:1536
	s_waitcnt lgkmcnt(3)
	v_mfma_f32_16x16x32_f16 v[44:47], v[64:67], v[60:63], v[44:47]
	global_load_dwordx4 v[64:67], v[12:13], off offset:1536
	global_load_dwordx4 v[84:87], v[14:15], off offset:1536
	s_waitcnt lgkmcnt(0)
	s_barrier
	ds_read_b128 v[88:91], v34 offset:32768
	v_mfma_f32_16x16x32_f16 v[52:55], v[72:75], v[60:63], v[52:55]
	ds_read_b128 v[60:63], v34 offset:36864
	ds_read_b128 v[72:75], v21 offset:16384
	ds_read_b128 v[92:95], v21 offset:20480
	s_waitcnt lgkmcnt(1)
	v_mfma_f32_16x16x32_f16 v[48:51], v[88:91], v[72:75], v[48:51]
	v_mfma_f32_16x16x32_f16 v[40:43], v[60:63], v[72:75], v[40:43]
	ds_read_b128 v[72:75], v36 offset:32768
	s_waitcnt lgkmcnt(1)
	v_mfma_f32_16x16x32_f16 v[44:47], v[88:91], v[92:95], v[44:47]
	v_mfma_f32_16x16x32_f16 v[52:55], v[60:63], v[92:95], v[52:55]
	ds_read_b128 v[60:63], v36 offset:36864
	ds_read_b128 v[88:91], v23 offset:16384
	ds_read_b128 v[92:95], v23 offset:20480
	s_waitcnt lgkmcnt(1)
	v_mfma_f32_16x16x32_f16 v[48:51], v[72:75], v[88:91], v[48:51]
	v_mfma_f32_16x16x32_f16 v[40:43], v[60:63], v[88:91], v[40:43]
	s_waitcnt lgkmcnt(0)
	v_mfma_f32_16x16x32_f16 v[44:47], v[72:75], v[92:95], v[44:47]
	ds_read_b128 v[72:75], v37 offset:32768
	ds_read_b128 v[88:91], v37 offset:36864
	v_mfma_f32_16x16x32_f16 v[52:55], v[60:63], v[92:95], v[52:55]
	ds_read_b128 v[60:63], v24 offset:16384
	ds_read_b128 v[92:95], v24 offset:20480
	s_waitcnt lgkmcnt(1)
	v_mfma_f32_16x16x32_f16 v[48:51], v[72:75], v[60:63], v[48:51]
	v_mfma_f32_16x16x32_f16 v[40:43], v[88:91], v[60:63], v[40:43]
	s_waitcnt lgkmcnt(0)
	v_mfma_f32_16x16x32_f16 v[44:47], v[72:75], v[92:95], v[44:47]
	ds_read_b128 v[60:63], v38 offset:32768
	ds_read_b128 v[72:75], v38 offset:36864
	v_mfma_f32_16x16x32_f16 v[52:55], v[88:91], v[92:95], v[52:55]
	ds_read_b128 v[88:91], v22 offset:16384
	ds_read_b128 v[92:95], v22 offset:20480
	global_load_dwordx4 v[96:99], v[16:17], off offset:1792
	global_load_dwordx4 v[100:103], v[18:19], off offset:1792
	s_waitcnt lgkmcnt(1)
	v_mfma_f32_16x16x32_f16 v[48:51], v[60:63], v[88:91], v[48:51]
	v_mfma_f32_16x16x32_f16 v[16:19], v[72:75], v[88:91], v[40:43]
	s_nop 2
	global_load_dwordx4 v[40:43], v[8:9], off offset:1792
	global_load_dwordx4 v[88:91], v[10:11], off offset:1792
	global_load_dwordx4 v[104:107], v[12:13], off offset:1792
	global_load_dwordx4 v[108:111], v[14:15], off offset:1792
	s_waitcnt vmcnt(11)
	ds_write_b128 v20, v[56:59]
	s_waitcnt vmcnt(10)
	ds_write_b128 v20, v[68:71] offset:8192
	s_waitcnt vmcnt(9)
	ds_write_b128 v20, v[76:79] offset:32768
	s_waitcnt vmcnt(8)
	ds_write_b128 v20, v[80:83] offset:40960
	s_waitcnt vmcnt(7)
	ds_write_b128 v20, v[64:67] offset:49152
	s_waitcnt vmcnt(6)
	ds_write_b128 v20, v[84:87] offset:57344
	s_waitcnt lgkmcnt(0)
	s_barrier
	ds_read_b128 v[12:15], v31 offset:32768
	v_mfma_f32_16x16x32_f16 v[8:11], v[60:63], v[92:95], v[44:47]
	v_mfma_f32_16x16x32_f16 v[44:47], v[72:75], v[92:95], v[52:55]
	s_nop 2
	ds_read_b128 v[52:55], v31 offset:36864
	ds_read_b128 v[56:59], v21
	ds_read_b128 v[60:63], v21 offset:4096
	s_waitcnt lgkmcnt(1)
	v_mfma_f32_16x16x32_f16 v[48:51], v[12:15], v[56:59], v[48:51]
	v_mfma_f32_16x16x32_f16 v[16:19], v[52:55], v[56:59], v[16:19]
	s_waitcnt lgkmcnt(0)
	v_mfma_f32_16x16x32_f16 v[8:11], v[12:15], v[60:63], v[8:11]
	ds_read_b128 v[12:15], v32 offset:32768
	ds_read_b128 v[56:59], v32 offset:36864
	v_mfma_f32_16x16x32_f16 v[44:47], v[52:55], v[60:63], v[44:47]
	ds_read_b128 v[52:55], v23
	ds_read_b128 v[60:63], v23 offset:4096
	s_waitcnt lgkmcnt(1)
	v_mfma_f32_16x16x32_f16 v[48:51], v[12:15], v[52:55], v[48:51]
	v_mfma_f32_16x16x32_f16 v[16:19], v[56:59], v[52:55], v[16:19]
	s_waitcnt lgkmcnt(0)
	v_mfma_f32_16x16x32_f16 v[8:11], v[12:15], v[60:63], v[8:11]
	ds_read_b128 v[12:15], v35 offset:32768
	ds_read_b128 v[52:55], v35 offset:36864
	v_mfma_f32_16x16x32_f16 v[44:47], v[56:59], v[60:63], v[44:47]
	ds_read_b128 v[56:59], v24
	ds_read_b128 v[60:63], v24 offset:4096
	s_waitcnt lgkmcnt(1)
	v_mfma_f32_16x16x32_f16 v[48:51], v[12:15], v[56:59], v[48:51]
	s_waitcnt lgkmcnt(0)
	v_mfma_f32_16x16x32_f16 v[8:11], v[12:15], v[60:63], v[8:11]
	ds_read_b128 v[12:15], v33 offset:32768
	v_mfma_f32_16x16x32_f16 v[16:19], v[52:55], v[56:59], v[16:19]
	v_mfma_f32_16x16x32_f16 v[44:47], v[52:55], v[60:63], v[44:47]
	ds_read_b128 v[52:55], v33 offset:36864
	ds_read_b128 v[56:59], v22
	ds_read_b128 v[60:63], v22 offset:4096
	s_waitcnt vmcnt(5)
	ds_write_b128 v20, v[96:99] offset:16384
	s_waitcnt vmcnt(4)
	ds_write_b128 v20, v[100:103] offset:24576
	s_waitcnt lgkmcnt(3)
	v_mfma_f32_16x16x32_f16 v[48:51], v[12:15], v[56:59], v[48:51]
	s_waitcnt lgkmcnt(2)
	v_mfma_f32_16x16x32_f16 v[8:11], v[12:15], v[60:63], v[8:11]
	v_add_u32_e32 v12, 0x10000, v20
	s_waitcnt vmcnt(3)
	ds_write_b128 v12, v[40:43]
	s_waitcnt vmcnt(2)
	ds_write_b128 v12, v[88:91] offset:8192
	s_waitcnt vmcnt(1)
	ds_write_b128 v12, v[104:107] offset:16384
	s_waitcnt vmcnt(0)
	ds_write_b128 v12, v[108:111] offset:24576
	s_waitcnt lgkmcnt(0)
	s_barrier
	ds_read_b128 v[12:15], v34 offset:32768
	v_mfma_f32_16x16x32_f16 v[16:19], v[52:55], v[56:59], v[16:19]
	v_mfma_f32_16x16x32_f16 v[40:43], v[52:55], v[60:63], v[44:47]
	ds_read_b128 v[32:35], v34 offset:36864
	s_nop 1
	ds_read_b128 v[44:47], v21 offset:16384
	ds_read_b128 v[52:55], v21 offset:20480
	s_waitcnt lgkmcnt(1)
	v_mfma_f32_16x16x32_f16 v[48:51], v[12:15], v[44:47], v[48:51]
	s_waitcnt lgkmcnt(0)
	v_mfma_f32_16x16x32_f16 v[8:11], v[12:15], v[52:55], v[8:11]
	ds_read_b128 v[12:15], v36 offset:32768
	v_mfma_f32_16x16x32_f16 v[16:19], v[32:35], v[44:47], v[16:19]
	v_mfma_f32_16x16x32_f16 v[32:35], v[32:35], v[52:55], v[40:43]
	s_nop 2
	ds_read_b128 v[40:43], v36 offset:36864
	ds_read_b128 v[44:47], v23 offset:16384
	ds_read_b128 v[52:55], v23 offset:20480
	s_waitcnt lgkmcnt(1)
	v_mfma_f32_16x16x32_f16 v[48:51], v[12:15], v[44:47], v[48:51]
	s_waitcnt lgkmcnt(0)
	v_mfma_f32_16x16x32_f16 v[8:11], v[12:15], v[52:55], v[8:11]
	ds_read_b128 v[12:15], v37 offset:32768
	v_mfma_f32_16x16x32_f16 v[16:19], v[40:43], v[44:47], v[16:19]
	v_mfma_f32_16x16x32_f16 v[32:35], v[40:43], v[52:55], v[32:35]
	ds_read_b128 v[40:43], v37 offset:36864
	ds_read_b128 v[44:47], v24 offset:16384
	ds_read_b128 v[52:55], v24 offset:20480
	v_lshlrev_b32_e32 v24, 6, v30
	s_waitcnt lgkmcnt(1)
	v_mfma_f32_16x16x32_f16 v[48:51], v[12:15], v[44:47], v[48:51]
	s_waitcnt lgkmcnt(0)
	v_mfma_f32_16x16x32_f16 v[8:11], v[12:15], v[52:55], v[8:11]
	ds_read_b128 v[12:15], v38 offset:32768
	v_mfma_f32_16x16x32_f16 v[16:19], v[40:43], v[44:47], v[16:19]
	v_mfma_f32_16x16x32_f16 v[32:35], v[40:43], v[52:55], v[32:35]
	ds_read_b128 v[36:39], v38 offset:36864
	ds_read_b128 v[40:43], v22 offset:16384
	ds_read_b128 v[44:47], v22 offset:20480
	s_waitcnt lgkmcnt(1)
	v_mfma_f32_16x16x32_f16 v[20:23], v[12:15], v[40:43], v[48:51]
	s_waitcnt lgkmcnt(0)
	v_mfma_f32_16x16x32_f16 v[12:15], v[12:15], v[44:47], v[8:11]
	s_nop 2
	v_lshl_add_u64 v[8:9], s[0:1], 0, v[24:25]
	v_lshlrev_b32_e32 v24, 3, v29
	v_mfma_f32_16x16x32_f16 v[16:19], v[36:39], v[40:43], v[16:19]
	v_lshl_add_u64 v[30:31], v[8:9], 0, v[24:25]
	v_mfma_f32_16x16x32_f16 v[8:11], v[36:39], v[44:47], v[32:35]
	v_mbcnt_lo_u32_b32 v196, -1, 0
	v_mbcnt_hi_u32_b32 v196, -1, v196
	v_and_b32_e32 v197, 15, v196
	v_lshrrev_b32_e32 v198, 4, v196
	v_lshrrev_b32_e32 v222, 10, v116
	s_nop 0
	v_readfirstlane_b32 s36, v222
	s_nop 3
	s_and_b32 s36, s36, 7
	s_mulk_i32 s36, 0x500
	s_add_u32 s36, s36, 0x8000
	v_mul_u32_u24_e32 v199, 0x50, v197
	v_lshl_add_u32 v199, v198, 3, v199
	v_add_u32_e32 v199, s36, v199
	v_lshrrev_b32_e32 v200, 2, v196
	v_and_b32_e32 v201, 3, v196
	v_mul_u32_u24_e32 v202, 0x50, v200
	v_lshl_add_u32 v202, v201, 4, v202
	v_add_u32_e32 v202, s36, v202
	v_lshlrev_b32_e32 v203, 2, v200
	v_add_u32_e32 v204, 32, v203
	v_lshlrev_b32_e32 v220, 4, v201
	v_mov_b32_e32 v221, 0
	v_sub_u32_e32 v205, v27, v197
	v_add_u32_e32 v205, v205, v200
	s_mov_b64 s[0:1], exec
	s_cbranch_execz .LBB7_9
	v_mov_b32_e32 v29, v25
	v_lshl_add_u64 v[24:25], s[2:3], 0, v[28:29]
	global_load_dword v24, v[24:25], off
	s_nop 0
	v_add_f32_e32 v16, v0, v16
	v_add_f32_e32 v17, v1, v17
	v_add_f32_e32 v18, v2, v18
	v_add_f32_e32 v19, v3, v19
	v_add_f32_e32 v20, v4, v20
	v_add_f32_e32 v21, v5, v21
	v_max_f32_e32 v25, 0, v16
	v_max_f32_e32 v28, 0, v17
	v_max_f32_e32 v18, 0, v18
	v_max_f32_e32 v19, 0, v19
	v_add_f32_e32 v22, v6, v22
	v_add_f32_e32 v23, v7, v23
	v_max_f32_e32 v20, 0, v20
	v_max_f32_e32 v21, 0, v21
	v_cvt_pk_f16_f32 v19, v18, v19
	v_cvt_pk_f16_f32 v18, v25, v28
	v_max_f32_e32 v22, 0, v22
	v_max_f32_e32 v23, 0, v23
	v_cvt_pk_f16_f32 v16, v20, v21
	v_cvt_pk_f16_f32 v17, v22, v23
	s_waitcnt vmcnt(0)
	v_ashrrev_i32_e32 v25, 31, v24
	v_lshlrev_b64 v[20:21], 11, v[24:25]
	v_lshl_add_u64 v[20:21], v[30:31], 0, v[20:21]
	ds_write_b64 v199, v[16:17]
	ds_write_b64 v199, v[18:19] offset:32
	ds_read_b128 v[208:211], v202
	ds_bpermute_b32 v216, v203, v20
	ds_bpermute_b32 v217, v203, v21
	v_add_u32_e32 v222, 0, v205
	v_cmp_gt_u32_e64 s[38:39], s4, v222
